# k_final: per-round slot/colsum/fragment loads issued together (was one dependent chain per load); first block fragments fetched before the barriers
# speedup vs baseline: 1.0103x; 1.0103x over previous
_Z7k_finalPK15HIP_vector_typeIfLj4EES2_PKiS4_PKfS6_PKDF16_Pf:
	s_load_dwordx4 s[4:7], s[0:1], 0x0
	s_load_dwordx2 s[8:9], s[0:1], 0x10
	s_load_dwordx2 s[12:13], s[0:1], 0x20
	s_load_dwordx2 s[28:29], s[0:1], 0x18
	s_load_dwordx2 s[30:31], s[0:1], 0x28
	s_load_dwordx2 s[18:19], s[0:1], 0x30
	s_lshl_b32 s3, s2, 5
	s_and_b32 s3, s3, 0xe0
	s_lshr_b32 s10, s2, 3
	s_add_i32 s16, s3, s10
	s_lshl_b32 s3, s16, 6
	v_and_b32_e32 v143, 31, v0
	v_or_b32_e32 v136, s3, v143
	v_mov_b32_e32 v137, 0
	s_waitcnt lgkmcnt(0)
	v_lshl_add_u64 v[10:11], v[136:137], 4, s[6:7]
	global_load_dwordx3 v[160:162], v[10:11], off
	global_load_dwordx3 v[164:166], v[10:11], off offset:512
	s_lshl_b32 s6, s16, 2
	s_lshr_b32 s14, s16, 6
	s_load_dword s9, s[8:9], s6 offset:0x0
	v_readfirstlane_b32 s15, v0
	s_lshl_b32 s8, s14, 12
	v_cmp_gt_u32_e64 s[6:7], 64, v0
	v_mov_b32_e32 v144, 0
	v_mov_b32_e32 v163, 0
	s_and_saveexec_b64 s[20:21], s[6:7]
	s_cbranch_execz .Lfin_tid64
	s_and_b32 s3, s3, 0xfc0
	v_or_b32_e32 v1, s3, v0
	v_or_b32_e32 v10, s8, v1
	v_lshlrev_b32_e32 v10, 2, v10
	global_load_dword v163, v10, s[28:29]
	global_load_dword v144, v10, s[30:31]
.Lfin_tid64:
	s_or_b64 exec, exec, s[20:21]
	v_add_u32_e32 v140, 0x600, v0
	v_max_i32_e32 v1, 0x600, v140
	s_mov_b32 s17, 0
	s_waitcnt lgkmcnt(0)
	v_cmp_gt_i32_e32 vcc, s9, v1
	s_and_saveexec_b64 s[20:21], vcc
	s_cbranch_execz .LBB1_6
	s_and_b32 s2, s2, 7
	s_mov_b32 s11, s17
	s_lshl_b32 s22, s2, 21
	s_lshl_b64 s[2:3], s[10:11], 16
	s_add_u32 s2, s22, s2
	s_addc_u32 s3, 0, s3
	s_add_u32 s2, s4, s2
	v_lshlrev_b32_e32 v136, 4, v0
	v_mov_b32_e32 v137, 0
	s_addc_u32 s3, s5, s3
	v_lshl_add_u64 v[10:11], s[2:3], 0, v[136:137]
	s_mov_b64 s[2:3], 0x600c
	v_lshl_add_u64 v[10:11], v[10:11], 0, s[2:3]
	s_mov_b64 s[2:3], 0
	s_mov_b64 s[10:11], 0x2000
	v_mov_b32_e32 v1, v140

.LBB1_9:
	v_and_b32_e32 v1, 63, v0
	s_lshr_b32 s20, s15, 6
	s_andn2_b64 vcc, exec, s[0:1]
	s_mov_b32 s15, 0
	s_cbranch_vccnz .LBB1_36
	s_lshl_b64 s[0:1], s[14:15], 19
	s_add_u32 s0, s18, s0
	s_addc_u32 s1, s19, s1
	v_lshlrev_b32_e32 v18, 4, v143
	v_mov_b32_e32 v19, 0
	v_lshl_add_u64 v[138:139], s[0:1], 0, v[18:19]
	s_lshl_b64 s[0:1], s[16:17], 16
	s_lshl_b32 s14, s20, 2
	s_add_u32 s16, s4, s0
	v_lshlrev_b32_e32 v9, 1, v0
	s_addc_u32 s17, s5, s1
	s_lshr_b32 s0, 0x73261540, s14
	v_and_b32_e32 v5, 19, v0
	v_and_b32_e32 v9, 8, v9
	v_lshrrev_b32_e32 v11, 1, v0
	v_cmp_gt_u32_e64 s[2:3], 32, v1
	s_lshl_b32 s1, s0, 5
	v_or_b32_e32 v10, v9, v5
	v_and_b32_e32 v11, 4, v11
	v_lshlrev_b32_e32 v2, 2, v0
	s_and_b32 s1, s1, 0xe0
	v_and_b32_e32 v3, 32, v0
	v_add_u32_e32 v149, 0x23900, v2
	v_exp_f32_e32 v150, 0xc0b8aa2f
	v_or_b32_e32 v151, 0x20800, v2
	s_xor_b32 s21, s1, 0xff
	v_or3_b32 v152, v10, v11, s1
	v_lshl_or_b32 v4, s1, 2, v3
	v_or_b32_e32 v154, 0x22000, v2
	v_or3_b32 v2, v5, s1, v9
	s_movk_i32 s1, 0x100
	s_and_b32 s0, s0, 7
	v_or3_b32 v155, v2, v11, s1
	v_lshl_or_b32 v2, s0, 7, v3
	v_mov_b32_e32 v18, v19
	v_mov_b32_e32 v32, v19
	v_mov_b32_e32 v33, v19
	v_or_b32_e32 v153, 0x22000, v4
	v_or_b32_e32 v156, 0x20800, v2
	v_mov_b32_e32 v20, v19
	v_mov_b32_e32 v21, v19
	v_mov_b32_e32 v22, v19
	v_mov_b32_e32 v23, v19
	v_mov_b32_e32 v24, v19
	v_mov_b32_e32 v25, v19
	v_mov_b32_e32 v26, v19
	v_mov_b32_e32 v27, v19
	v_mov_b32_e32 v28, v19
	v_mov_b32_e32 v29, v19
	v_mov_b32_e32 v30, v19
	v_mov_b32_e32 v31, v19
	v_mov_b64_e32 v[64:65], v[32:33]
	v_mov_b64_e32 v[80:81], v[32:33]
	v_mov_b64_e32 v[48:49], v[32:33]
	v_mov_b64_e32 v[2:3], v[18:19]
	v_cmp_eq_u32_e64 s[4:5], 0, v1
	s_add_i32 s14, s14, 0x23a00
	v_or_b32_e32 v142, 0x200, v0
	v_or_b32_e32 v141, 0x400, v0
	v_mov_b32_e32 v157, 0x23a00
	v_mov_b32_e32 v158, 0x23a10
	s_mov_b32 s22, 0x44800000
	v_mov_b32_e32 v159, 0xff800000
	v_mov_b64_e32 v[62:63], v[30:31]
	v_mov_b64_e32 v[60:61], v[28:29]
	v_mov_b64_e32 v[58:59], v[26:27]
	v_mov_b64_e32 v[56:57], v[24:25]
	v_mov_b64_e32 v[54:55], v[22:23]
	v_mov_b64_e32 v[52:53], v[20:21]
	v_mov_b64_e32 v[50:51], v[18:19]
	v_mov_b64_e32 v[78:79], v[30:31]
	v_mov_b64_e32 v[76:77], v[28:29]
	v_mov_b64_e32 v[74:75], v[26:27]
	v_mov_b64_e32 v[72:73], v[24:25]
	v_mov_b64_e32 v[70:71], v[22:23]
	v_mov_b64_e32 v[68:69], v[20:21]
	v_mov_b64_e32 v[66:67], v[18:19]
	v_mov_b64_e32 v[46:47], v[30:31]
	v_mov_b64_e32 v[44:45], v[28:29]
	v_mov_b64_e32 v[42:43], v[26:27]
	v_mov_b64_e32 v[40:41], v[24:25]
	v_mov_b64_e32 v[38:39], v[22:23]
	v_mov_b64_e32 v[36:37], v[20:21]
	v_mov_b64_e32 v[34:35], v[18:19]
	v_mov_b64_e32 v[4:5], v[20:21]
	v_mov_b64_e32 v[6:7], v[22:23]
	v_mov_b64_e32 v[8:9], v[24:25]
	v_mov_b64_e32 v[10:11], v[26:27]
	v_mov_b64_e32 v[12:13], v[28:29]
	v_mov_b64_e32 v[14:15], v[30:31]
	v_mov_b64_e32 v[16:17], v[32:33]
	v_mov_b32_e32 v32, 0
	s_cmp_eq_u32 s15, 0
	s_cselect_b64 s[0:1], -1, 0
	s_and_b64 vcc, exec, s[0:1]
	s_cbranch_vccnz .LBB1_12

.LBB1_12:
	s_sub_i32 s23, s9, s15
	s_min_i32 s23, s23, 0x600
	v_cmp_gt_i32_e32 vcc, s23, v0
	v_cmp_gt_i32_e64 s[34:35], s23, v142
	v_cmp_gt_i32_e64 s[36:37], s23, v141
	v_cmp_gt_i32_e64 s[38:39], s23, v152
	v_and_b32_e32 v26, 0x3ff, v153
	v_lshrrev_b32_e32 v26, 2, v26
	v_add_u32_e32 v27, 16, v26
	v_cmp_gt_i32_e64 s[40:41], s23, v26
	v_cmp_gt_i32_e64 s[42:43], s23, v27
	v_cndmask_b32_e32 v20, 0, v0, vcc
	v_cndmask_b32_e64 v21, 0, v142, s[34:35]
	v_cndmask_b32_e64 v22, 0, v141, s[36:37]
	v_cndmask_b32_e64 v23, 0, v152, s[38:39]
	v_cndmask_b32_e64 v26, 0, v26, s[40:41]
	v_cndmask_b32_e64 v27, 0, v27, s[42:43]
	v_add_lshl_u32 v20, v20, s15, 4
	v_add_lshl_u32 v21, v21, s15, 4
	v_add_lshl_u32 v22, v22, s15, 4
	v_add_lshl_u32 v23, v23, s15, 4
	v_add_lshl_u32 v26, v26, s15, 4
	v_add_lshl_u32 v27, v27, s15, 4
	global_load_dword v24, v20, s[16:17] offset:12
	global_load_dword v25, v21, s[16:17] offset:12
	global_load_dword v28, v22, s[16:17] offset:12
	global_load_dword v29, v26, s[16:17] offset:12
	global_load_dword v30, v27, s[16:17] offset:12
	global_load_dwordx3 v[96:98], v23, s[16:17]
	v_mov_b32_e32 v83, 0
	v_mov_b32_e32 v85, 0
	s_waitcnt vmcnt(1)
	v_cndmask_b32_e32 v24, 0, v24, vcc
	v_cndmask_b32_e64 v25, 0, v25, s[34:35]
	v_cndmask_b32_e64 v28, 0, v28, s[36:37]
	v_add_lshl_u32 v20, v24, s8, 2
	v_add_lshl_u32 v21, v25, s8, 2
	v_add_lshl_u32 v22, v28, s8, 2
	global_load_dword v20, v20, s[12:13]
	global_load_dword v21, v21, s[12:13]
	global_load_dword v22, v22, s[12:13]
	v_ashrrev_i32_e32 v29, 3, v29
	v_ashrrev_i32_e32 v30, 3, v30
	v_lshlrev_b32_e32 v82, 10, v29
	v_lshlrev_b32_e32 v84, 10, v30
	v_lshl_add_u64 v[82:83], v[138:139], 0, v[82:83]
	v_lshl_add_u64 v[84:85], v[138:139], 0, v[84:85]
	global_load_dwordx4 v[126:129], v[82:83], off
	global_load_dwordx4 v[122:125], v[82:83], off offset:512
	global_load_dwordx4 v[118:121], v[84:85], off
	global_load_dwordx4 v[114:117], v[84:85], off offset:512
	ds_write_b32 v154, v24
	ds_write_b32 v154, v25 offset:2048
	ds_write_b32 v154, v28 offset:4096
	s_waitcnt vmcnt(4)
	v_rcp_f32_e32 v24, v20
	v_rcp_f32_e32 v25, v21
	v_rcp_f32_e32 v28, v22
	v_cmp_lt_f32_e64 s[44:45], 0, v20
	v_cmp_lt_f32_e64 s[46:47], 0, v21
	v_cmp_lt_f32_e64 s[48:49], 0, v22
	s_and_b64 s[44:45], s[44:45], vcc
	s_and_b64 s[46:47], s[46:47], s[34:35]
	s_and_b64 s[48:49], s[48:49], s[36:37]
	v_cndmask_b32_e64 v20, 0, v24, s[44:45]
	v_cndmask_b32_e64 v21, 0, v25, s[46:47]
	v_cndmask_b32_e64 v18, 0, v28, s[48:49]
	v_max_f32_e32 v23, v20, v20
	v_max_f32_e32 v24, v137, v137
	v_max_f32_e32 v23, v24, v23
	v_max3_f32 v137, v23, v21, v18
	s_andn2_b64 vcc, exec, s[0:1]
	s_cbranch_vccnz .LBB1_24
	v_mov_b32_e32 v22, 0
	v_max_f32_e32 v23, v137, v137
	v_mov_b32_e32 v24, 0
	v_mov_b32_dpp v22, v137 quad_perm:[1,0,3,2] row_mask:0xf bank_mask:0xf
	v_max_f32_e32 v22, v22, v22
	v_max_f32_e32 v22, v23, v22
	v_mov_b32_e32 v23, 0
	s_nop 1
	v_mov_b32_dpp v23, v22 quad_perm:[2,3,0,1] row_mask:0xf bank_mask:0xf
	v_max_f32_e32 v23, v23, v23
	v_max_f32_e32 v22, v22, v23
	v_mov_b32_e32 v23, 0
	s_nop 1
	v_mov_b32_dpp v23, v22 row_half_mirror row_mask:0xf bank_mask:0xf
	s_nop 1
	v_mov_b32_dpp v24, v23 quad_perm:[3,2,1,0] row_mask:0xf bank_mask:0xf
	v_max_f32_e32 v23, v24, v24
	v_max_f32_e32 v22, v22, v23
	v_mov_b32_e32 v23, 0
	s_nop 1
	v_mov_b32_dpp v23, v22 row_ror:8 row_mask:0xf bank_mask:0xf
	v_max_f32_e32 v23, v23, v23
	v_max_f32_e32 v22, v22, v23
	s_nop 0
	v_readlane_b32 s18, v22, 32
	v_readlane_b32 s19, v22, 48
	v_readlane_b32 s0, v22, 0
	v_readlane_b32 s1, v22, 16
	v_max_f32_e64 v22, s19, s19
	v_max_f32_e64 v23, s18, s18
	v_max_f32_e32 v22, v23, v22
	v_mov_b32_e32 v23, s1
	v_max3_f32 v137, s0, v23, v22
	s_and_saveexec_b64 s[0:1], s[4:5]
	v_mov_b32_e32 v22, s14
	ds_write_b32 v22, v137
	s_or_b64 exec, exec, s[0:1]
	s_waitcnt lgkmcnt(0)
	s_barrier
	ds_read_b128 v[22:25], v157
	ds_read_b128 v[26:29], v158
	s_waitcnt lgkmcnt(1)
	v_max_f32_e32 v23, v23, v23
	v_max_f32_e32 v22, v22, v22
	v_max_f32_e32 v22, v22, v23
	v_max3_f32 v22, v22, v24, v25
	s_waitcnt lgkmcnt(0)
	v_max3_f32 v22, v22, v26, v27
	v_max3_f32 v22, v22, v28, v29
	v_div_scale_f32 v23, s[0:1], v22, v22, s22
	v_rcp_f32_e32 v24, v23
	v_cmp_lt_f32_e64 s[0:1], 0, v22
	v_fma_f32 v25, -v23, v24, 1.0
	v_fmac_f32_e32 v24, v25, v24
	v_div_scale_f32 v25, vcc, s22, v22, s22
	v_mul_f32_e32 v26, v25, v24
	v_fma_f32 v27, -v23, v26, v25
	v_fmac_f32_e32 v26, v27, v24
	v_fma_f32 v23, -v23, v26, v25
	v_div_fmas_f32 v23, v23, v24, v26
	s_and_saveexec_b64 s[18:19], s[6:7]
	v_mul_f32_e32 v24, 0x3a800000, v22
	v_mul_f32_e32 v24, v144, v24
	v_mul_f32_e32 v24, v150, v24
	ds_write_b32 v149, v24
	v_add_u32_e32 v25, 0xffffff00, v149
	ds_write_b32 v25, v163
	s_or_b64 exec, exec, s[18:19]
	v_div_fixup_f32 v22, v23, v22, s22
	v_cndmask_b32_e64 v147, v165, v164, s[2:3]
	v_cndmask_b32_e64 v148, v166, 1.0, s[2:3]
	v_cndmask_b32_e64 v145, v161, v160, s[2:3]
	v_cndmask_b32_e64 v146, v162, 1.0, s[2:3]
	v_cndmask_b32_e64 v32, 0, v22, s[0:1]
.LBB1_24:
	s_add_i32 s0, s21, s23
	v_mul_f32_e32 v18, v32, v18
	s_ashr_i32 s0, s0, 8
	ds_write_b32 v151, v18 offset:4096
	v_med3_i32 v18, s0, 0, 6
	v_mul_f32_e32 v20, v32, v20
	v_readfirstlane_b32 s24, v18
	s_cmp_gt_i32 s24, 0
	v_mul_f32_e32 v21, v32, v21
	s_cselect_b64 s[18:19], -1, 0
	s_cmp_lt_i32 s24, 1
	ds_write2st64_b32 v151, v20, v21 offset1:8
	s_waitcnt lgkmcnt(0)
	s_barrier
	s_cbranch_scc1 .LBB1_32
	s_and_b64 s[0:1], s[38:39], exec
	s_andn2_b64 vcc, exec, s[18:19]
	s_cbranch_vccnz .LBB1_33

.LBB1_36:
	s_waitcnt vmcnt(0)
	s_and_saveexec_b64 s[18:19], s[6:7]
	v_mov_b32_e32 v2, 0x23800
	v_lshl_or_b32 v2, v0, 2, v2
	ds_write_b32 v2, v163
	s_or_b64 exec, exec, s[18:19]
	v_mov_b32_e32 v2, 0
	v_mov_b32_e32 v16, v2
	v_mov_b32_e32 v17, v2
	v_mov_b32_e32 v3, v2
	v_mov_b32_e32 v4, v2
	v_mov_b32_e32 v5, v2
	v_mov_b32_e32 v6, v2
	v_mov_b32_e32 v7, v2
	v_mov_b32_e32 v8, v2
	v_mov_b32_e32 v9, v2
	v_mov_b32_e32 v10, v2
	v_mov_b32_e32 v11, v2
	v_mov_b32_e32 v12, v2
	v_mov_b32_e32 v13, v2
	v_mov_b32_e32 v14, v2
	v_mov_b32_e32 v15, v2
	v_mov_b64_e32 v[48:49], v[16:17]
	v_mov_b64_e32 v[80:81], v[16:17]
	v_mov_b64_e32 v[64:65], v[16:17]
	v_mov_b64_e32 v[46:47], v[14:15]
	v_mov_b64_e32 v[44:45], v[12:13]
	v_mov_b64_e32 v[42:43], v[10:11]
	v_mov_b64_e32 v[40:41], v[8:9]
	v_mov_b64_e32 v[38:39], v[6:7]
	v_mov_b64_e32 v[36:37], v[4:5]
	v_mov_b64_e32 v[34:35], v[2:3]
	v_mov_b64_e32 v[78:79], v[14:15]
	v_mov_b64_e32 v[76:77], v[12:13]
	v_mov_b64_e32 v[74:75], v[10:11]
	v_mov_b64_e32 v[72:73], v[8:9]
	v_mov_b64_e32 v[70:71], v[6:7]
	v_mov_b64_e32 v[68:69], v[4:5]
	v_mov_b64_e32 v[66:67], v[2:3]
	v_mov_b64_e32 v[62:63], v[14:15]
	v_mov_b64_e32 v[60:61], v[12:13]
	v_mov_b64_e32 v[58:59], v[10:11]
	v_mov_b64_e32 v[56:57], v[8:9]
	v_mov_b64_e32 v[54:55], v[6:7]
	v_mov_b64_e32 v[52:53], v[4:5]
	v_mov_b64_e32 v[50:51], v[2:3]
